# v67 + prep_moe deal: light workgroups convert all six item slots behind their in-proj units (none ahead), so every workgroup starts the GEMM together
# baseline (speedup 1.0000x reference)
; __device__ __forceinline__ void phase_prep_moe(Frame& F, int l, int part) {
;     ...
;     const int nextra = ((T / 256) * (INP / 256)) % F.G, nlight = F.G - nextra;
;     const int slots = (nextra ? nextra : 0) * NWAVES + nlight * NWAVES * (nextra ? 5 : 1);
;     const bool light = F.bx >= nextra; const int mult = (light && nextra) ? 5 : 1;
;     const int base = light ? nextra * NWAVES + ((F.bx - nextra) * NWAVES + F.wave) * mult : F.bx * NWAVES + F.wave;
;     const int k0 = part ? 1 : 0, k1 = part ? mult : 1;
;     for (int rnd = 0; rnd * slots < NEXP * I_E; ++rnd)
;       for (int k = k0; k < k1; ++k) {
;         const int it = rnd * slots + base + k; if (it >= NEXP * I_E) break;
.LBB0_289:
	s_cmp_eq_u32 s70, 1
	s_cselect_b32 s8, 1, 0
	s_mov_b64 s[10:11], 0
	s_and_b64 vcc, exec, s[80:81]
	s_cbranch_vccnz .LBB0_597
.LBB0_290:
	s_xor_b64 s[80:81], s[10:11], -1
	s_add_u32 s2, s74, 0x3e00000
	v_lshlrev_b32_e32 v0, 2, v67
	s_addc_u32 s3, s75, 0
	v_lshrrev_b32_e32 v69, 4, v67
	v_and_b32_e32 v66, 60, v0
	s_add_u32 s6, s74, 0x5e00000
	v_lshlrev_b32_e32 v0, 2, v66
	v_mul_u32_u24_e32 v2, 0x104, v69
	s_addc_u32 s7, s75, 0
	v_add3_u32 v106, s78, v0, v2
	v_lshlrev_b32_e32 v2, 3, v67
	s_and_b64 s[12:13], s[10:11], exec
	v_lshrrev_b32_e32 v0, 3, v67
	v_and_b32_e32 v68, 56, v2
	s_cselect_b32 s9, 1, s70
	s_cmp_eq_u32 s70, 1
	s_cselect_b32 s12, 1, 0
	s_and_b32 s13, s10, 1
	s_cmp_lg_u32 s13, 0
	s_cselect_b32 s9, s12, s70
	v_mul_u32_u24_e32 v2, 0x104, v68
	v_lshlrev_b32_e32 v3, 2, v0
	s_cmp_lg_u32 s9, s8
	v_add3_u32 v107, s78, v2, v3
	v_or_b32_e32 v2, 8, v0
	v_or_b32_e32 v3, 16, v0
	v_or_b32_e32 v4, 24, v0
	v_or_b32_e32 v5, 32, v0
	v_or_b32_e32 v6, 40, v0
	v_or_b32_e32 v7, 48, v0
	v_or_b32_e32 v8, 56, v0
	s_cselect_b64 s[12:13], -1, 0
	v_lshlrev_b32_e32 v70, 9, v0
	v_mov_b32_e32 v71, v1
	v_lshlrev_b32_e32 v72, 9, v2
	v_mov_b32_e32 v73, v1
	v_lshlrev_b32_e32 v74, 9, v3
	v_mov_b32_e32 v75, v1
	v_lshlrev_b32_e32 v76, 9, v4
	v_mov_b32_e32 v77, v1
	v_lshlrev_b32_e32 v78, 9, v5
	v_mov_b32_e32 v79, v1
	v_lshlrev_b32_e32 v80, 9, v6
	v_mov_b32_e32 v81, v1
	v_lshlrev_b32_e32 v82, 9, v7
	v_mov_b32_e32 v83, v1
	v_lshlrev_b32_e32 v84, 9, v8
	v_mov_b32_e32 v85, v1
	v_lshlrev_b32_e32 v86, 11, v0
	v_mov_b32_e32 v87, v1
	v_lshlrev_b32_e32 v88, 11, v2
	v_mov_b32_e32 v89, v1
	v_lshlrev_b32_e32 v90, 11, v3
	v_mov_b32_e32 v91, v1
	v_lshlrev_b32_e32 v92, 11, v4
	v_mov_b32_e32 v93, v1
	v_lshlrev_b32_e32 v94, 11, v5
	v_mov_b32_e32 v95, v1
	v_lshlrev_b32_e32 v96, 11, v6
	v_mov_b32_e32 v97, v1
	v_lshlrev_b32_e32 v98, 11, v7
	v_mov_b32_e32 v99, v1
	v_lshlrev_b32_e32 v100, 11, v8
	v_mov_b32_e32 v101, v1
	s_sub_i32 s20, s9, s8
	s_add_i32 s21, s71, s8
	s_mov_b32 s8, 0
	v_add_u32_e32 v108, 0x410, v106
	v_add_u32_e32 v109, 0x418, v106
	v_add_u32_e32 v110, 0x820, v106
	s_mov_b32 s26, 0
	s_branch .LBB0_292
